# prologue rebalance + fp8 GEMM epilogue trims (dead cvt zero-inits, unneeded 32-state nop pads) + dilated O readback batched + final grid barrier skipped
# speedup vs baseline: 1.0053x; 1.0053x over previous
.LBB0_405:
	s_or_b64 exec, exec, s[94:95]
	ds_read_b128 v[26:29], v223
	ds_read_b128 v[30:33], v224
	ds_read_b128 v[34:37], v225
	ds_read_b128 v[38:41], v226
	v_readlane_b32 s0, v255, 24
	v_lshlrev_b64 v[2:3], 26, v[2:3]
	v_readlane_b32 s1, v255, 25
	s_lshl_b64 s[72:73], s[74:75], 23
	s_lshl_b32 s84, s83, 7
	v_lshl_add_u64 v[2:3], s[0:1], 0, v[2:3]
	v_lshl_add_u64 v[2:3], v[2:3], 0, s[72:73]
	v_lshl_add_u64 v[2:3], v[2:3], 0, s[84:85]
	v_mov_b32_e32 v151, v163
	v_or_b32_e32 v8, s81, v199
	v_lshl_add_u64 v[6:7], v[2:3], 0, v[150:151]
	v_lshlrev_b32_e32 v8, s33, v8
	v_add_u32_e32 v8, s80, v8
	v_ashrrev_i32_e32 v9, 31, v8
	v_lshlrev_b64 v[8:9], 10, v[8:9]
	v_lshl_add_u64 v[8:9], v[6:7], 0, v[8:9]
	s_waitcnt lgkmcnt(3)
	global_store_dwordx4 v[8:9], v[26:29], off nt
	v_or_b32_e32 v8, s81, v207
	v_lshlrev_b32_e32 v8, s33, v8
	v_add_u32_e32 v8, s80, v8
	v_ashrrev_i32_e32 v9, 31, v8
	v_lshlrev_b64 v[8:9], 10, v[8:9]
	v_lshl_add_u64 v[8:9], v[6:7], 0, v[8:9]
	s_waitcnt lgkmcnt(2)
	global_store_dwordx4 v[8:9], v[30:33], off nt
	v_or_b32_e32 v8, s81, v208
	v_lshlrev_b32_e32 v8, s33, v8
	v_add_u32_e32 v8, s80, v8
	v_ashrrev_i32_e32 v9, 31, v8
	v_lshlrev_b64 v[8:9], 10, v[8:9]
	v_lshl_add_u64 v[8:9], v[6:7], 0, v[8:9]
	s_waitcnt lgkmcnt(1)
	global_store_dwordx4 v[8:9], v[34:37], off nt
	v_or_b32_e32 v8, s81, v209
	v_lshlrev_b32_e32 v8, s33, v8
	v_add_u32_e32 v8, s80, v8
	v_ashrrev_i32_e32 v9, 31, v8
	v_lshlrev_b64 v[8:9], 10, v[8:9]
	s_add_i32 s71, s71, s3
	v_lshl_add_u64 v[6:7], v[6:7], 0, v[8:9]
	s_mov_b32 s72, s3
	s_cmpk_lt_i32 s79, 0x1800
	s_waitcnt lgkmcnt(0)
	global_store_dwordx4 v[6:7], v[38:41], off nt
	s_cbranch_scc0 .LBB0_412

.LBB0_1307:
	v_pk_mul_f32 v[8:9], v[154:155], s[2:3] op_sel_hi:[1,0]
	v_pk_mul_f32 v[12:13], v[146:147], s[2:3] op_sel_hi:[1,0]
	v_exp_f32_e32 v8, v8
	v_exp_f32_e32 v9, v9
	v_exp_f32_e32 v12, v12
	v_exp_f32_e32 v13, v13
	v_pk_mul_f32 v[16:17], v[138:139], s[2:3] op_sel_hi:[1,0]
	v_pk_mul_f32 v[20:21], v[130:131], s[2:3] op_sel_hi:[1,0]
	v_exp_f32_e32 v16, v16
	v_exp_f32_e32 v17, v17
	v_exp_f32_e32 v20, v20
	v_exp_f32_e32 v21, v21
	v_pk_fma_f32 v[8:9], v[8:9], s[82:83], s[82:83] op_sel_hi:[1,0,0]
	v_pk_fma_f32 v[12:13], v[12:13], s[82:83], s[82:83] op_sel_hi:[1,0,0]
	v_rcp_f32_e32 v8, v8
	v_rcp_f32_e32 v9, v9
	v_rcp_f32_e32 v12, v12
	v_rcp_f32_e32 v13, v13
	v_pk_fma_f32 v[16:17], v[16:17], s[82:83], s[82:83] op_sel_hi:[1,0,0]
	v_pk_fma_f32 v[20:21], v[20:21], s[82:83], s[82:83] op_sel_hi:[1,0,0]
	v_rcp_f32_e32 v16, v16
	v_rcp_f32_e32 v17, v17
	v_pk_mul_f32 v[2:3], v[154:155], v[158:159]
	v_rcp_f32_e32 v20, v20
	v_rcp_f32_e32 v21, v21
	v_pk_mul_f32 v[2:3], v[2:3], v[8:9]
	v_pk_mul_f32 v[8:9], v[156:157], s[2:3] op_sel_hi:[1,0]
	v_pk_mul_f32 v[10:11], v[146:147], v[150:151]
	v_exp_f32_e32 v8, v8
	v_exp_f32_e32 v9, v9
	v_pk_mul_f32 v[10:11], v[10:11], v[12:13]
	v_pk_mul_f32 v[12:13], v[148:149], s[2:3] op_sel_hi:[1,0]
	v_pk_mul_f32 v[14:15], v[138:139], v[142:143]
	v_exp_f32_e32 v12, v12
	v_exp_f32_e32 v13, v13
	v_pk_mul_f32 v[14:15], v[14:15], v[16:17]
	v_pk_mul_f32 v[16:17], v[140:141], s[2:3] op_sel_hi:[1,0]
	v_pk_mul_f32 v[18:19], v[130:131], v[134:135]
	v_exp_f32_e32 v16, v16
	v_exp_f32_e32 v17, v17
	v_pk_mul_f32 v[18:19], v[18:19], v[20:21]
	v_pk_mul_f32 v[20:21], v[132:133], s[2:3] op_sel_hi:[1,0]
	v_pk_fma_f32 v[8:9], v[8:9], s[82:83], s[82:83] op_sel_hi:[1,0,0]
	v_exp_f32_e32 v20, v20
	v_exp_f32_e32 v21, v21
	v_rcp_f32_e32 v8, v8
	v_rcp_f32_e32 v9, v9
	v_pk_fma_f32 v[12:13], v[12:13], s[82:83], s[82:83] op_sel_hi:[1,0,0]
	v_pk_fma_f32 v[16:17], v[16:17], s[82:83], s[82:83] op_sel_hi:[1,0,0]
	v_rcp_f32_e32 v12, v12
	v_rcp_f32_e32 v13, v13
	v_rcp_f32_e32 v16, v16
	v_rcp_f32_e32 v17, v17
	v_pk_fma_f32 v[20:21], v[20:21], s[82:83], s[82:83] op_sel_hi:[1,0,0]
	v_pk_mul_f32 v[6:7], v[156:157], v[160:161]
	v_rcp_f32_e32 v20, v20
	v_rcp_f32_e32 v21, v21
	v_pk_mul_f32 v[8:9], v[6:7], v[8:9]
	v_pk_mul_f32 v[6:7], v[148:149], v[152:153]
	v_lshl_add_u32 v4, s54, 8, v178
	v_pk_mul_f32 v[12:13], v[6:7], v[12:13]
	v_pk_mul_f32 v[6:7], v[140:141], v[144:145]
	s_lshl_b32 s24, s55, 7
	v_pk_mul_f32 v[16:17], v[6:7], v[16:17]
	v_pk_mul_f32 v[6:7], v[132:133], v[136:137]
	s_ashr_i32 s25, s24, 31
	v_pk_mul_f32 v[20:21], v[6:7], v[20:21]
	v_cvt_pk_fp8_f32 v6, v2, v3
	v_or_b32_e32 v2, v4, v179
	v_cvt_pk_fp8_f32 v7, v10, v11
	v_cvt_pk_fp8_f32 v6, v8, v9 op_sel:[0,0,1]
	v_cvt_pk_fp8_f32 v8, v14, v15
	v_cvt_pk_fp8_f32 v9, v18, v19
	v_ashrrev_i32_e32 v3, 31, v2
	v_lshlrev_b64 v[2:3], 11, v[2:3]
	v_lshl_add_u64 v[2:3], s[10:11], 0, v[2:3]
	v_lshl_add_u64 v[2:3], v[2:3], 0, s[24:25]
	v_cvt_pk_fp8_f32 v7, v12, v13 op_sel:[0,0,1]
	v_cvt_pk_fp8_f32 v8, v16, v17 op_sel:[0,0,1]
	v_cvt_pk_fp8_f32 v9, v20, v21 op_sel:[0,0,1]
	v_lshl_add_u64 v[2:3], v[2:3], 0, s[84:85]
	s_nop 1
	v_permlane16_swap_b32 v6, v8
	s_nop 1
	v_permlane16_swap_b32 v7, v9
	v_lshl_add_u64 v[2:3], v[2:3], 0, v[170:171]
	global_store_dwordx4 v[2:3], v[6:9], off nt
	v_pk_mul_f32 v[12:13], v[114:115], s[2:3] op_sel_hi:[1,0]
	v_pk_mul_f32 v[16:17], v[106:107], s[2:3] op_sel_hi:[1,0]
	v_pk_mul_f32 v[8:9], v[122:123], s[2:3] op_sel_hi:[1,0]
	v_exp_f32_e32 v12, v12
	v_exp_f32_e32 v8, v8
	v_exp_f32_e32 v9, v9
	v_exp_f32_e32 v13, v13
	v_exp_f32_e32 v16, v16
	v_exp_f32_e32 v17, v17
	v_pk_mul_f32 v[20:21], v[98:99], s[2:3] op_sel_hi:[1,0]
	v_pk_fma_f32 v[8:9], v[8:9], s[82:83], s[82:83] op_sel_hi:[1,0,0]
	v_exp_f32_e32 v20, v20
	v_exp_f32_e32 v21, v21
	v_rcp_f32_e32 v8, v8
	v_rcp_f32_e32 v9, v9
	v_pk_fma_f32 v[12:13], v[12:13], s[82:83], s[82:83] op_sel_hi:[1,0,0]
	v_pk_fma_f32 v[16:17], v[16:17], s[82:83], s[82:83] op_sel_hi:[1,0,0]
	v_rcp_f32_e32 v12, v12
	v_rcp_f32_e32 v13, v13
	v_rcp_f32_e32 v16, v16
	v_rcp_f32_e32 v17, v17
	v_pk_fma_f32 v[20:21], v[20:21], s[82:83], s[82:83] op_sel_hi:[1,0,0]
	v_pk_mul_f32 v[2:3], v[122:123], v[126:127]
	v_rcp_f32_e32 v20, v20
	v_rcp_f32_e32 v21, v21
	v_pk_mul_f32 v[2:3], v[2:3], v[8:9]
	v_pk_mul_f32 v[8:9], v[124:125], s[2:3] op_sel_hi:[1,0]
	v_pk_mul_f32 v[10:11], v[114:115], v[118:119]
	v_exp_f32_e32 v8, v8
	v_exp_f32_e32 v9, v9
	v_pk_mul_f32 v[10:11], v[10:11], v[12:13]
	v_pk_mul_f32 v[12:13], v[116:117], s[2:3] op_sel_hi:[1,0]
	v_pk_mul_f32 v[14:15], v[106:107], v[110:111]
	v_exp_f32_e32 v12, v12
	v_exp_f32_e32 v13, v13
	v_pk_mul_f32 v[14:15], v[14:15], v[16:17]
	v_pk_mul_f32 v[16:17], v[108:109], s[2:3] op_sel_hi:[1,0]
	v_pk_mul_f32 v[18:19], v[98:99], v[102:103]
	v_exp_f32_e32 v16, v16
	v_exp_f32_e32 v17, v17
	v_pk_mul_f32 v[18:19], v[18:19], v[20:21]
	v_pk_mul_f32 v[20:21], v[100:101], s[2:3] op_sel_hi:[1,0]
	v_pk_fma_f32 v[8:9], v[8:9], s[82:83], s[82:83] op_sel_hi:[1,0,0]
	v_exp_f32_e32 v20, v20
	v_exp_f32_e32 v21, v21
	v_rcp_f32_e32 v8, v8
	v_rcp_f32_e32 v9, v9
	v_pk_fma_f32 v[12:13], v[12:13], s[82:83], s[82:83] op_sel_hi:[1,0,0]
	v_pk_fma_f32 v[16:17], v[16:17], s[82:83], s[82:83] op_sel_hi:[1,0,0]
	v_rcp_f32_e32 v12, v12
	v_rcp_f32_e32 v13, v13
	v_rcp_f32_e32 v16, v16
	v_rcp_f32_e32 v17, v17
	v_pk_fma_f32 v[20:21], v[20:21], s[82:83], s[82:83] op_sel_hi:[1,0,0]
	v_pk_mul_f32 v[6:7], v[124:125], v[128:129]
	v_rcp_f32_e32 v20, v20
	v_rcp_f32_e32 v21, v21
	v_pk_mul_f32 v[8:9], v[6:7], v[8:9]
	v_pk_mul_f32 v[6:7], v[116:117], v[120:121]
	s_and_b64 vcc, exec, s[0:1]
	v_pk_mul_f32 v[12:13], v[6:7], v[12:13]
	v_pk_mul_f32 v[6:7], v[108:109], v[112:113]
	s_nop 0
	v_pk_mul_f32 v[16:17], v[6:7], v[16:17]
	v_pk_mul_f32 v[6:7], v[100:101], v[104:105]
	s_nop 0
	v_pk_mul_f32 v[20:21], v[6:7], v[20:21]
	v_cvt_pk_fp8_f32 v6, v2, v3
	v_or_b32_e32 v2, v4, v199
	v_cvt_pk_fp8_f32 v7, v10, v11
	v_cvt_pk_fp8_f32 v6, v8, v9 op_sel:[0,0,1]
	v_cvt_pk_fp8_f32 v8, v14, v15
	v_cvt_pk_fp8_f32 v9, v18, v19
	v_ashrrev_i32_e32 v3, 31, v2
	v_lshlrev_b64 v[2:3], 11, v[2:3]
	v_lshl_add_u64 v[2:3], s[10:11], 0, v[2:3]
	v_lshl_add_u64 v[2:3], v[2:3], 0, s[24:25]
	v_cvt_pk_fp8_f32 v7, v12, v13 op_sel:[0,0,1]
	v_cvt_pk_fp8_f32 v8, v16, v17 op_sel:[0,0,1]
	v_cvt_pk_fp8_f32 v9, v20, v21 op_sel:[0,0,1]
	v_lshl_add_u64 v[2:3], v[2:3], 0, s[84:85]
	s_nop 1
	v_permlane16_swap_b32 v6, v8
	s_nop 1
	v_permlane16_swap_b32 v7, v9
	v_lshl_add_u64 v[2:3], v[2:3], 0, v[170:171]
	global_store_dwordx4 v[2:3], v[6:9], off nt
	v_pk_mul_f32 v[12:13], v[82:83], s[2:3] op_sel_hi:[1,0]
	v_pk_mul_f32 v[16:17], v[74:75], s[2:3] op_sel_hi:[1,0]
	v_pk_mul_f32 v[8:9], v[90:91], s[2:3] op_sel_hi:[1,0]
	v_exp_f32_e32 v12, v12
	v_exp_f32_e32 v8, v8
	v_exp_f32_e32 v9, v9
	v_exp_f32_e32 v13, v13
	v_exp_f32_e32 v16, v16
	v_exp_f32_e32 v17, v17
	v_pk_mul_f32 v[20:21], v[66:67], s[2:3] op_sel_hi:[1,0]
	v_pk_fma_f32 v[8:9], v[8:9], s[82:83], s[82:83] op_sel_hi:[1,0,0]
	v_exp_f32_e32 v20, v20
	v_exp_f32_e32 v21, v21
	v_rcp_f32_e32 v8, v8
	v_rcp_f32_e32 v9, v9
	v_pk_fma_f32 v[12:13], v[12:13], s[82:83], s[82:83] op_sel_hi:[1,0,0]
	v_pk_fma_f32 v[16:17], v[16:17], s[82:83], s[82:83] op_sel_hi:[1,0,0]
	v_rcp_f32_e32 v12, v12
	v_rcp_f32_e32 v13, v13
	v_rcp_f32_e32 v16, v16
	v_rcp_f32_e32 v17, v17
	v_pk_fma_f32 v[20:21], v[20:21], s[82:83], s[82:83] op_sel_hi:[1,0,0]
	v_pk_mul_f32 v[2:3], v[90:91], v[94:95]
	v_rcp_f32_e32 v20, v20
	v_rcp_f32_e32 v21, v21
	v_pk_mul_f32 v[2:3], v[2:3], v[8:9]
	v_pk_mul_f32 v[8:9], v[92:93], s[2:3] op_sel_hi:[1,0]
	v_pk_mul_f32 v[10:11], v[82:83], v[86:87]
	v_exp_f32_e32 v8, v8
	v_exp_f32_e32 v9, v9
	v_pk_mul_f32 v[10:11], v[10:11], v[12:13]
	v_pk_mul_f32 v[12:13], v[84:85], s[2:3] op_sel_hi:[1,0]
	v_pk_mul_f32 v[14:15], v[74:75], v[78:79]
	v_exp_f32_e32 v12, v12
	v_exp_f32_e32 v13, v13
	v_pk_mul_f32 v[14:15], v[14:15], v[16:17]
	v_pk_mul_f32 v[16:17], v[76:77], s[2:3] op_sel_hi:[1,0]
	v_pk_mul_f32 v[18:19], v[66:67], v[70:71]
	v_exp_f32_e32 v16, v16
	v_exp_f32_e32 v17, v17
	v_pk_mul_f32 v[18:19], v[18:19], v[20:21]
	v_pk_mul_f32 v[20:21], v[68:69], s[2:3] op_sel_hi:[1,0]
	v_pk_fma_f32 v[8:9], v[8:9], s[82:83], s[82:83] op_sel_hi:[1,0,0]
	v_exp_f32_e32 v20, v20
	v_exp_f32_e32 v21, v21
	v_rcp_f32_e32 v8, v8
	v_rcp_f32_e32 v9, v9
	v_pk_fma_f32 v[12:13], v[12:13], s[82:83], s[82:83] op_sel_hi:[1,0,0]
	v_pk_fma_f32 v[16:17], v[16:17], s[82:83], s[82:83] op_sel_hi:[1,0,0]
	v_rcp_f32_e32 v12, v12
	v_rcp_f32_e32 v13, v13
	v_rcp_f32_e32 v16, v16
	v_rcp_f32_e32 v17, v17
	v_pk_fma_f32 v[20:21], v[20:21], s[82:83], s[82:83] op_sel_hi:[1,0,0]
	v_pk_mul_f32 v[6:7], v[92:93], v[96:97]
	v_rcp_f32_e32 v20, v20
	v_rcp_f32_e32 v21, v21
	v_pk_mul_f32 v[8:9], v[6:7], v[8:9]
	v_pk_mul_f32 v[6:7], v[84:85], v[88:89]
	v_add_u32_e32 v4, 0x80, v4
	v_pk_mul_f32 v[12:13], v[6:7], v[12:13]
	v_pk_mul_f32 v[6:7], v[76:77], v[80:81]
	s_nop 0
	v_pk_mul_f32 v[16:17], v[6:7], v[16:17]
	v_pk_mul_f32 v[6:7], v[68:69], v[72:73]
	s_nop 0
	v_pk_mul_f32 v[20:21], v[6:7], v[20:21]
	v_cvt_pk_fp8_f32 v6, v2, v3
	v_or_b32_e32 v2, v4, v179
	v_cvt_pk_fp8_f32 v7, v10, v11
	v_cvt_pk_fp8_f32 v6, v8, v9 op_sel:[0,0,1]
	v_cvt_pk_fp8_f32 v8, v14, v15
	v_cvt_pk_fp8_f32 v9, v18, v19
	v_ashrrev_i32_e32 v3, 31, v2
	v_lshlrev_b64 v[2:3], 11, v[2:3]
	v_lshl_add_u64 v[2:3], s[10:11], 0, v[2:3]
	v_lshl_add_u64 v[2:3], v[2:3], 0, s[24:25]
	v_cvt_pk_fp8_f32 v7, v12, v13 op_sel:[0,0,1]
	v_cvt_pk_fp8_f32 v8, v16, v17 op_sel:[0,0,1]
	v_cvt_pk_fp8_f32 v9, v20, v21 op_sel:[0,0,1]
	v_lshl_add_u64 v[2:3], v[2:3], 0, s[84:85]
	s_nop 1
	v_permlane16_swap_b32 v6, v8
	s_nop 1
	v_permlane16_swap_b32 v7, v9
	v_lshl_add_u64 v[2:3], v[2:3], 0, v[170:171]
	global_store_dwordx4 v[2:3], v[6:9], off nt
	v_pk_mul_f32 v[12:13], v[50:51], s[2:3] op_sel_hi:[1,0]
	v_pk_mul_f32 v[16:17], v[42:43], s[2:3] op_sel_hi:[1,0]
	v_pk_mul_f32 v[8:9], v[58:59], s[2:3] op_sel_hi:[1,0]
	v_exp_f32_e32 v12, v12
	v_exp_f32_e32 v8, v8
	v_exp_f32_e32 v9, v9
	v_exp_f32_e32 v13, v13
	v_exp_f32_e32 v16, v16
	v_exp_f32_e32 v17, v17
	v_pk_mul_f32 v[20:21], v[34:35], s[2:3] op_sel_hi:[1,0]
	v_pk_fma_f32 v[8:9], v[8:9], s[82:83], s[82:83] op_sel_hi:[1,0,0]
	v_exp_f32_e32 v20, v20
	v_exp_f32_e32 v21, v21
	v_rcp_f32_e32 v8, v8
	v_rcp_f32_e32 v9, v9
	v_pk_fma_f32 v[12:13], v[12:13], s[82:83], s[82:83] op_sel_hi:[1,0,0]
	v_pk_fma_f32 v[16:17], v[16:17], s[82:83], s[82:83] op_sel_hi:[1,0,0]
	v_rcp_f32_e32 v12, v12
	v_rcp_f32_e32 v13, v13
	v_rcp_f32_e32 v16, v16
	v_rcp_f32_e32 v17, v17
	v_pk_fma_f32 v[20:21], v[20:21], s[82:83], s[82:83] op_sel_hi:[1,0,0]
	v_pk_mul_f32 v[2:3], v[58:59], v[62:63]
	v_rcp_f32_e32 v20, v20
	v_rcp_f32_e32 v21, v21
	v_pk_mul_f32 v[2:3], v[2:3], v[8:9]
	v_pk_mul_f32 v[8:9], v[60:61], s[2:3] op_sel_hi:[1,0]
	v_pk_mul_f32 v[10:11], v[50:51], v[54:55]
	v_exp_f32_e32 v8, v8
	v_exp_f32_e32 v9, v9
	v_pk_mul_f32 v[10:11], v[10:11], v[12:13]
	v_pk_mul_f32 v[12:13], v[52:53], s[2:3] op_sel_hi:[1,0]
	v_pk_mul_f32 v[14:15], v[42:43], v[46:47]
	v_exp_f32_e32 v12, v12
	v_exp_f32_e32 v13, v13
	v_pk_mul_f32 v[14:15], v[14:15], v[16:17]
	v_pk_mul_f32 v[16:17], v[44:45], s[2:3] op_sel_hi:[1,0]
	v_pk_mul_f32 v[18:19], v[34:35], v[38:39]
	v_exp_f32_e32 v16, v16
	v_exp_f32_e32 v17, v17
	v_pk_mul_f32 v[18:19], v[18:19], v[20:21]
	v_pk_mul_f32 v[20:21], v[36:37], s[2:3] op_sel_hi:[1,0]
	v_pk_fma_f32 v[8:9], v[8:9], s[82:83], s[82:83] op_sel_hi:[1,0,0]
	v_exp_f32_e32 v20, v20
	v_exp_f32_e32 v21, v21
	v_rcp_f32_e32 v8, v8
	v_rcp_f32_e32 v9, v9
	v_pk_fma_f32 v[12:13], v[12:13], s[82:83], s[82:83] op_sel_hi:[1,0,0]
	v_pk_fma_f32 v[16:17], v[16:17], s[82:83], s[82:83] op_sel_hi:[1,0,0]
	v_rcp_f32_e32 v12, v12
	v_rcp_f32_e32 v13, v13
	v_rcp_f32_e32 v16, v16
	v_rcp_f32_e32 v17, v17
	v_pk_fma_f32 v[20:21], v[20:21], s[82:83], s[82:83] op_sel_hi:[1,0,0]
	v_pk_mul_f32 v[6:7], v[60:61], v[64:65]
	v_rcp_f32_e32 v20, v20
	v_rcp_f32_e32 v21, v21
	v_pk_mul_f32 v[8:9], v[6:7], v[8:9]
	v_pk_mul_f32 v[6:7], v[52:53], v[56:57]
	s_nop 0
	v_pk_mul_f32 v[12:13], v[6:7], v[12:13]
	v_pk_mul_f32 v[6:7], v[44:45], v[48:49]
	s_nop 0
	v_pk_mul_f32 v[16:17], v[6:7], v[16:17]
	v_pk_mul_f32 v[6:7], v[36:37], v[40:41]
	s_nop 0
	v_pk_mul_f32 v[20:21], v[6:7], v[20:21]
	v_cvt_pk_fp8_f32 v6, v2, v3
	v_or_b32_e32 v2, v4, v199
	v_ashrrev_i32_e32 v3, 31, v2
	v_cvt_pk_fp8_f32 v6, v8, v9 op_sel:[0,0,1]
	v_cvt_pk_fp8_f32 v7, v10, v11
	v_cvt_pk_fp8_f32 v8, v14, v15
	v_cvt_pk_fp8_f32 v9, v18, v19
	v_lshlrev_b64 v[2:3], 11, v[2:3]
	v_lshl_add_u64 v[2:3], s[10:11], 0, v[2:3]
	v_lshl_add_u64 v[2:3], v[2:3], 0, s[24:25]
	v_lshl_add_u64 v[2:3], v[2:3], 0, s[84:85]
	v_cvt_pk_fp8_f32 v7, v12, v13 op_sel:[0,0,1]
	v_cvt_pk_fp8_f32 v8, v16, v17 op_sel:[0,0,1]
	v_cvt_pk_fp8_f32 v9, v20, v21 op_sel:[0,0,1]
	v_lshl_add_u64 v[2:3], v[2:3], 0, v[170:171]
	s_mov_b64 s[24:25], -1
	s_nop 1
	v_permlane16_swap_b32 v6, v8
	s_nop 1
	v_permlane16_swap_b32 v7, v9
	global_store_dwordx4 v[2:3], v[6:9], off nt
	s_cbranch_vccnz .LBB0_1292
	s_andn2_b64 vcc, exec, s[8:9]
	s_cbranch_vccnz .LBB0_1291
	s_barrier
	s_branch .LBB0_1291

.LBB0_1377:
	v_lshl_add_u32 v12, s18, 8, v199
	v_or_b32_e32 v2, v12, v200
	v_ashrrev_i32_e32 v3, 31, v2
	v_lshlrev_b64 v[6:7], 10, v[2:3]
	v_pk_mul_f32 v[8:9], v[158:159], s[86:87] op_sel_hi:[1,0]
	v_cvt_pk_fp8_f32 v2, v8, v9
	v_pk_mul_f32 v[8:9], v[154:155], s[86:87] op_sel_hi:[1,0]
	v_cvt_pk_fp8_f32 v3, v8, v9
	v_pk_mul_f32 v[4:5], v[160:161], s[86:87] op_sel_hi:[1,0]
	v_pk_mul_f32 v[10:11], v[150:151], s[86:87] op_sel_hi:[1,0]
	v_cvt_pk_fp8_f32 v2, v4, v5 op_sel:[0,0,1]
	v_pk_mul_f32 v[4:5], v[156:157], s[86:87] op_sel_hi:[1,0]
	s_lshl_b32 s18, s19, 8
	v_cvt_pk_fp8_f32 v3, v4, v5 op_sel:[0,0,1]
	v_cvt_pk_fp8_f32 v4, v10, v11
	v_pk_mul_f32 v[10:11], v[146:147], s[86:87] op_sel_hi:[1,0]
	v_cvt_pk_fp8_f32 v5, v10, v11
	s_ashr_i32 s19, s18, 31
	v_lshl_add_u64 v[6:7], s[6:7], 0, v[6:7]
	v_pk_mul_f32 v[8:9], v[152:153], s[86:87] op_sel_hi:[1,0]
	v_lshl_add_u64 v[6:7], v[6:7], 0, s[18:19]
	v_cvt_pk_fp8_f32 v4, v8, v9 op_sel:[0,0,1]
	v_pk_mul_f32 v[8:9], v[148:149], s[86:87] op_sel_hi:[1,0]
	v_lshl_add_u64 v[6:7], v[6:7], 0, s[84:85]
	v_cvt_pk_fp8_f32 v5, v8, v9 op_sel:[0,0,1]
	s_nop 1
	v_permlane16_swap_b32 v2, v4
	v_lshl_add_u64 v[6:7], v[6:7], 0, v[166:167]
	s_nop 1
	v_permlane16_swap_b32 v3, v5
	global_store_dwordx4 v[6:7], v[2:5], off
	v_pk_mul_f32 v[8:9], v[142:143], s[86:87] op_sel_hi:[1,0]
	v_pk_mul_f32 v[10:11], v[134:135], s[86:87] op_sel_hi:[1,0]
	v_cvt_pk_fp8_f32 v2, v8, v9
	v_pk_mul_f32 v[8:9], v[138:139], s[86:87] op_sel_hi:[1,0]
	v_cvt_pk_fp8_f32 v3, v8, v9
	v_pk_mul_f32 v[4:5], v[144:145], s[86:87] op_sel_hi:[1,0]
	v_pk_mul_f32 v[8:9], v[136:137], s[86:87] op_sel_hi:[1,0]
	v_cvt_pk_fp8_f32 v2, v4, v5 op_sel:[0,0,1]
	v_pk_mul_f32 v[4:5], v[140:141], s[86:87] op_sel_hi:[1,0]
	s_and_b64 vcc, exec, s[0:1]
	v_cvt_pk_fp8_f32 v3, v4, v5 op_sel:[0,0,1]
	v_cvt_pk_fp8_f32 v4, v10, v11
	v_pk_mul_f32 v[10:11], v[130:131], s[86:87] op_sel_hi:[1,0]
	v_cvt_pk_fp8_f32 v5, v10, v11
	v_cvt_pk_fp8_f32 v4, v8, v9 op_sel:[0,0,1]
	v_pk_mul_f32 v[8:9], v[132:133], s[86:87] op_sel_hi:[1,0]
	s_nop 1
	v_permlane16_swap_b32 v2, v4
	v_pk_mul_f32 v[10:11], v[118:119], s[86:87] op_sel_hi:[1,0]
	v_cvt_pk_fp8_f32 v5, v8, v9 op_sel:[0,0,1]
	v_pk_mul_f32 v[8:9], v[126:127], s[86:87] op_sel_hi:[1,0]
	s_nop 1
	v_permlane16_swap_b32 v3, v5
	global_store_dwordx4 v[6:7], v[2:5], off offset:128
	s_nop 1
	v_or_b32_e32 v2, v12, v201
	v_ashrrev_i32_e32 v3, 31, v2
	v_lshlrev_b64 v[6:7], 10, v[2:3]
	v_cvt_pk_fp8_f32 v2, v8, v9
	v_pk_mul_f32 v[8:9], v[122:123], s[86:87] op_sel_hi:[1,0]
	v_cvt_pk_fp8_f32 v3, v8, v9
	v_pk_mul_f32 v[4:5], v[128:129], s[86:87] op_sel_hi:[1,0]
	v_lshl_add_u64 v[6:7], s[6:7], 0, v[6:7]
	v_cvt_pk_fp8_f32 v2, v4, v5 op_sel:[0,0,1]
	v_pk_mul_f32 v[4:5], v[124:125], s[86:87] op_sel_hi:[1,0]
	v_pk_mul_f32 v[8:9], v[120:121], s[86:87] op_sel_hi:[1,0]
	v_cvt_pk_fp8_f32 v3, v4, v5 op_sel:[0,0,1]
	v_cvt_pk_fp8_f32 v4, v10, v11
	v_pk_mul_f32 v[10:11], v[114:115], s[86:87] op_sel_hi:[1,0]
	v_cvt_pk_fp8_f32 v5, v10, v11
	v_lshl_add_u64 v[6:7], v[6:7], 0, s[18:19]
	v_cvt_pk_fp8_f32 v4, v8, v9 op_sel:[0,0,1]
	v_pk_mul_f32 v[8:9], v[116:117], s[86:87] op_sel_hi:[1,0]
	v_lshl_add_u64 v[6:7], v[6:7], 0, s[84:85]
	v_cvt_pk_fp8_f32 v5, v8, v9 op_sel:[0,0,1]
	s_nop 1
	v_permlane16_swap_b32 v2, v4
	v_lshl_add_u64 v[6:7], v[6:7], 0, v[166:167]
	s_nop 1
	v_permlane16_swap_b32 v3, v5
	global_store_dwordx4 v[6:7], v[2:5], off
	v_pk_mul_f32 v[8:9], v[110:111], s[86:87] op_sel_hi:[1,0]
	v_pk_mul_f32 v[10:11], v[98:99], s[86:87] op_sel_hi:[1,0]
	v_cvt_pk_fp8_f32 v2, v8, v9
	v_pk_mul_f32 v[8:9], v[106:107], s[86:87] op_sel_hi:[1,0]
	v_cvt_pk_fp8_f32 v3, v8, v9
	v_pk_mul_f32 v[4:5], v[112:113], s[86:87] op_sel_hi:[1,0]
	v_pk_mul_f32 v[8:9], v[100:101], s[86:87] op_sel_hi:[1,0]
	v_cvt_pk_fp8_f32 v2, v4, v5 op_sel:[0,0,1]
	v_pk_mul_f32 v[4:5], v[108:109], s[86:87] op_sel_hi:[1,0]
	v_add_u32_e32 v12, 0x80, v12
	v_cvt_pk_fp8_f32 v3, v4, v5 op_sel:[0,0,1]
	v_cvt_pk_fp8_f32 v4, v10, v11
	v_pk_mul_f32 v[10:11], v[90:91], s[86:87] op_sel_hi:[1,0]
	v_cvt_pk_fp8_f32 v5, v10, v11
	v_cvt_pk_fp8_f32 v4, v8, v9 op_sel:[0,0,1]
	v_pk_mul_f32 v[8:9], v[92:93], s[86:87] op_sel_hi:[1,0]
	s_nop 1
	v_permlane16_swap_b32 v2, v4
	v_pk_mul_f32 v[10:11], v[86:87], s[86:87] op_sel_hi:[1,0]
	v_cvt_pk_fp8_f32 v5, v8, v9 op_sel:[0,0,1]
	v_pk_mul_f32 v[8:9], v[102:103], s[86:87] op_sel_hi:[1,0]
	s_nop 1
	v_permlane16_swap_b32 v3, v5
	global_store_dwordx4 v[6:7], v[2:5], off offset:128
	s_nop 1
	v_or_b32_e32 v2, v12, v200
	v_ashrrev_i32_e32 v3, 31, v2
	v_lshlrev_b64 v[6:7], 10, v[2:3]
	v_cvt_pk_fp8_f32 v2, v8, v9
	v_pk_mul_f32 v[8:9], v[94:95], s[86:87] op_sel_hi:[1,0]
	v_cvt_pk_fp8_f32 v3, v8, v9
	v_pk_mul_f32 v[4:5], v[104:105], s[86:87] op_sel_hi:[1,0]
	v_lshl_add_u64 v[6:7], s[6:7], 0, v[6:7]
	v_cvt_pk_fp8_f32 v2, v4, v5 op_sel:[0,0,1]
	v_pk_mul_f32 v[4:5], v[96:97], s[86:87] op_sel_hi:[1,0]
	v_pk_mul_f32 v[8:9], v[88:89], s[86:87] op_sel_hi:[1,0]
	v_cvt_pk_fp8_f32 v3, v4, v5 op_sel:[0,0,1]
	v_cvt_pk_fp8_f32 v4, v10, v11
	v_pk_mul_f32 v[10:11], v[82:83], s[86:87] op_sel_hi:[1,0]
	v_cvt_pk_fp8_f32 v5, v10, v11
	v_lshl_add_u64 v[6:7], v[6:7], 0, s[18:19]
	v_cvt_pk_fp8_f32 v4, v8, v9 op_sel:[0,0,1]
	v_pk_mul_f32 v[8:9], v[84:85], s[86:87] op_sel_hi:[1,0]
	v_lshl_add_u64 v[6:7], v[6:7], 0, s[84:85]
	v_cvt_pk_fp8_f32 v5, v8, v9 op_sel:[0,0,1]
	s_nop 1
	v_permlane16_swap_b32 v2, v4
	v_lshl_add_u64 v[6:7], v[6:7], 0, v[166:167]
	s_nop 1
	v_permlane16_swap_b32 v3, v5
	global_store_dwordx4 v[6:7], v[2:5], off
	v_pk_mul_f32 v[8:9], v[78:79], s[86:87] op_sel_hi:[1,0]
	v_pk_mul_f32 v[10:11], v[70:71], s[86:87] op_sel_hi:[1,0]
	v_cvt_pk_fp8_f32 v2, v8, v9
	v_pk_mul_f32 v[8:9], v[74:75], s[86:87] op_sel_hi:[1,0]
	v_cvt_pk_fp8_f32 v3, v8, v9
	v_pk_mul_f32 v[4:5], v[80:81], s[86:87] op_sel_hi:[1,0]
	v_pk_mul_f32 v[8:9], v[72:73], s[86:87] op_sel_hi:[1,0]
	v_cvt_pk_fp8_f32 v2, v4, v5 op_sel:[0,0,1]
	v_pk_mul_f32 v[4:5], v[76:77], s[86:87] op_sel_hi:[1,0]
	s_nop 0
	v_cvt_pk_fp8_f32 v3, v4, v5 op_sel:[0,0,1]
	v_cvt_pk_fp8_f32 v4, v10, v11
	v_pk_mul_f32 v[10:11], v[66:67], s[86:87] op_sel_hi:[1,0]
	v_cvt_pk_fp8_f32 v5, v10, v11
	v_cvt_pk_fp8_f32 v4, v8, v9 op_sel:[0,0,1]
	v_pk_mul_f32 v[8:9], v[68:69], s[86:87] op_sel_hi:[1,0]
	s_nop 1
	v_permlane16_swap_b32 v2, v4
	v_pk_mul_f32 v[10:11], v[54:55], s[86:87] op_sel_hi:[1,0]
	v_cvt_pk_fp8_f32 v5, v8, v9 op_sel:[0,0,1]
	v_pk_mul_f32 v[8:9], v[62:63], s[86:87] op_sel_hi:[1,0]
	s_nop 1
	v_permlane16_swap_b32 v3, v5
	global_store_dwordx4 v[6:7], v[2:5], off offset:128
	s_nop 1
	v_or_b32_e32 v2, v12, v201
	v_ashrrev_i32_e32 v3, 31, v2
	v_lshlrev_b64 v[6:7], 10, v[2:3]
	v_cvt_pk_fp8_f32 v2, v8, v9
	v_pk_mul_f32 v[8:9], v[58:59], s[86:87] op_sel_hi:[1,0]
	v_cvt_pk_fp8_f32 v3, v8, v9
	v_pk_mul_f32 v[4:5], v[64:65], s[86:87] op_sel_hi:[1,0]
	v_lshl_add_u64 v[6:7], s[6:7], 0, v[6:7]
	v_cvt_pk_fp8_f32 v2, v4, v5 op_sel:[0,0,1]
	v_pk_mul_f32 v[4:5], v[60:61], s[86:87] op_sel_hi:[1,0]
	v_pk_mul_f32 v[8:9], v[56:57], s[86:87] op_sel_hi:[1,0]
	v_cvt_pk_fp8_f32 v3, v4, v5 op_sel:[0,0,1]
	v_cvt_pk_fp8_f32 v4, v10, v11
	v_pk_mul_f32 v[10:11], v[50:51], s[86:87] op_sel_hi:[1,0]
	v_cvt_pk_fp8_f32 v5, v10, v11
	v_lshl_add_u64 v[6:7], v[6:7], 0, s[18:19]
	v_cvt_pk_fp8_f32 v4, v8, v9 op_sel:[0,0,1]
	v_pk_mul_f32 v[8:9], v[52:53], s[86:87] op_sel_hi:[1,0]
	v_lshl_add_u64 v[6:7], v[6:7], 0, s[84:85]
	v_cvt_pk_fp8_f32 v5, v8, v9 op_sel:[0,0,1]
	s_nop 1
	v_permlane16_swap_b32 v2, v4
	v_lshl_add_u64 v[6:7], v[6:7], 0, v[166:167]
	s_nop 1
	v_permlane16_swap_b32 v3, v5
	global_store_dwordx4 v[6:7], v[2:5], off
	v_pk_mul_f32 v[8:9], v[46:47], s[86:87] op_sel_hi:[1,0]
	v_pk_mul_f32 v[10:11], v[38:39], s[86:87] op_sel_hi:[1,0]
	v_cvt_pk_fp8_f32 v2, v8, v9
	v_pk_mul_f32 v[8:9], v[42:43], s[86:87] op_sel_hi:[1,0]
	v_cvt_pk_fp8_f32 v3, v8, v9
	v_pk_mul_f32 v[4:5], v[48:49], s[86:87] op_sel_hi:[1,0]
	v_pk_mul_f32 v[8:9], v[40:41], s[86:87] op_sel_hi:[1,0]
	v_cvt_pk_fp8_f32 v2, v4, v5 op_sel:[0,0,1]
	v_pk_mul_f32 v[4:5], v[44:45], s[86:87] op_sel_hi:[1,0]
	s_mov_b64 s[18:19], -1
	v_cvt_pk_fp8_f32 v3, v4, v5 op_sel:[0,0,1]
	v_cvt_pk_fp8_f32 v4, v10, v11
	v_pk_mul_f32 v[10:11], v[34:35], s[86:87] op_sel_hi:[1,0]
	v_cvt_pk_fp8_f32 v5, v10, v11
	v_cvt_pk_fp8_f32 v4, v8, v9 op_sel:[0,0,1]
	v_pk_mul_f32 v[8:9], v[36:37], s[86:87] op_sel_hi:[1,0]
	s_nop 1
	v_permlane16_swap_b32 v2, v4
	s_nop 0
	v_cvt_pk_fp8_f32 v5, v8, v9 op_sel:[0,0,1]
	s_nop 0
	s_nop 1
	v_permlane16_swap_b32 v3, v5
	global_store_dwordx4 v[6:7], v[2:5], off offset:128
	s_cbranch_vccnz .LBB0_1364
	s_andn2_b64 vcc, exec, s[4:5]
	s_cbranch_vccnz .LBB0_1363
	s_barrier
	s_branch .LBB0_1363

.LBB0_1488:
	s_or_b64 exec, exec, s[8:9]
	s_waitcnt vmcnt(0)
	s_barrier
	v_readlane_b32 s100, v255, 16
	s_cmp_eq_u32 s100, 3
	s_cbranch_scc1 .LBB0_1531
	s_and_saveexec_b64 s[34:35], s[80:81]
	s_cbranch_execnz .LBB0_1489
	s_getpc_b64 s[98:99]
